# speedup vs baseline: 1.0219x; 1.0219x over previous
_Z11edge_kernelILi36ELb1EEvPKfS1_PKDF16_PKiS5_S1_S1_S1_S1_S1_PDF16_:
	s_load_dwordx8 s[4:11], s[0:1], 0x0
	s_load_dwordx8 s[12:19], s[0:1], 0x20
	s_load_dwordx4 s[20:23], s[0:1], 0x40
	s_load_dwordx2 s[24:25], s[0:1], 0x50
	v_readfirstlane_b32 s3, v0
	v_bfe_u32 v75, v0, 4, 2
	v_and_b32_e32 v76, 15, v0
	v_and_b32_e32 v78, 63, v0
	s_lshr_b32 s3, s3, 6
	s_lshl_b32 s2, s2, 1
	s_add_i32 s2, s2, s3
	v_lshlrev_b32_e32 v74, 8, v75
	v_lshl_or_b32 v74, v76, 4, v74
	v_lshlrev_b32_e32 v79, 4, v78
	v_lshl_or_b32 v77, v76, 2, v75
	v_lshlrev_b32_e32 v77, 2, v77
	v_mul_u32_u24_e32 v73, 0x900, v75
	v_lshl_or_b32 v73, v76, 4, v73
	v_mul_u32_u24_e32 v78, 36, v75
	s_mul_i32 s28, s2, 0x2400
	s_lshl_b32 s29, s2, 14
	s_lshl_b32 s30, s2, 2
	s_lshl_b32 s31, s2, 8
	s_lshl_b32 s33, s3, 10
	s_lshl_b32 s34, s3, 8
	s_addk_i32 s34, 0x4000
	s_waitcnt lgkmcnt(0)
	s_add_u32 s10, s10, s30
	s_addc_u32 s11, s11, 0
	s_add_u32 s12, s12, s30
	s_addc_u32 s13, s13, 0
	s_load_dword s35, s[10:11], 0x0
	s_load_dword s36, s[12:13], 0x0
	s_add_u32 s14, s14, s28
	s_addc_u32 s15, s15, 0
	global_load_dwordx4 v[0:3], v73, s[14:15] nt
	global_load_dwordx4 v[4:7], v73, s[14:15] offset:256 nt
	global_load_dwordx4 v[8:11], v73, s[14:15] offset:512 nt
	global_load_dwordx4 v[12:15], v73, s[14:15] offset:768 nt
	global_load_dwordx4 v[16:19], v73, s[14:15] offset:1024 nt
	global_load_dwordx4 v[20:23], v73, s[14:15] offset:1280 nt
	global_load_dwordx4 v[24:27], v73, s[14:15] offset:1536 nt
	global_load_dwordx4 v[28:31], v73, s[14:15] offset:1792 nt
	global_load_dwordx4 v[32:35], v73, s[14:15] offset:2048 nt
	s_add_u32 s22, s22, s33
	s_addc_u32 s23, s23, 0
	s_add_u32 s18, s18, s29
	s_addc_u32 s19, s19, 0
	s_mov_b32 m0, s33
	s_nop 0
	global_load_lds_dwordx4 v79, s[22:23]
	global_load_lds_dwordx4 v79, s[22:23] offset:2048
	s_add_u32 m0, m0, 0x1000
	s_add_u32 s22, s22, 0x1000
	s_addc_u32 s23, s23, 0
	global_load_lds_dwordx4 v79, s[22:23]
	global_load_lds_dwordx4 v79, s[22:23] offset:2048
	s_add_u32 m0, m0, 0x1000
	s_add_u32 s22, s22, 0x1000
	s_addc_u32 s23, s23, 0
	global_load_lds_dwordx4 v79, s[22:23]
	global_load_lds_dwordx4 v79, s[22:23] offset:2048
	s_add_u32 m0, m0, 0x1000
	s_add_u32 s22, s22, 0x1000
	s_addc_u32 s23, s23, 0
	global_load_lds_dwordx4 v79, s[22:23]
	global_load_lds_dwordx4 v79, s[22:23] offset:2048
	s_add_u32 s16, s16, s31
	s_addc_u32 s17, s17, 0
	s_add_u32 s20, s20, s31
	s_addc_u32 s21, s21, 0
	s_waitcnt lgkmcnt(0)
	s_lshl_b32 s36, s36, 7
	s_add_u32 s24, s24, s36
	s_addc_u32 s25, s25, 0
	s_lshl_b32 s37, s35, 7
	s_lshl_b32 s38, s35, 4
	s_add_u32 s4, s4, s37
	s_addc_u32 s5, s5, 0
	s_add_u32 s6, s6, s38
	s_addc_u32 s7, s7, 0
	v_mov_b32_e32 v93, 0
	v_mov_b32_e32 v92, v78
	v_lshl_add_u64 v[94:95], s[4:5], 0, v[92:93]
	v_lshl_add_u64 v[94:95], v[94:95], 0, 20
	v_cmp_eq_u32_e32 vcc, 3, v75
	s_nop 1
	v_mov_b32_e32 v90, s6
	v_mov_b32_e32 v91, s7
	v_cndmask_b32_e32 v94, v94, v90, vcc
	v_cndmask_b32_e32 v95, v95, v91, vcc
	global_load_dwordx4 v[80:83], v78, s[4:5] nt
	global_load_dword v84, v78, s[4:5] offset:16 nt
	global_load_dwordx4 v[86:89], v[94:95], off nt
	global_load_dword v72, v77, s[16:17] nt
	global_load_dword v64, v77, s[20:21] nt
	global_load_dword v63, v93, s[24:25]
	v_add_u32_e32 v78, s34, v77
	v_lshl_add_u32 v79, v75, 2, s34
	s_waitcnt vmcnt(3)
	s_barrier
	v_pk_mul_f32 v[96:97], v[80:81], v[0:1] op_sel_hi:[0,1]
	v_pk_mul_f32 v[98:99], v[80:81], v[2:3] op_sel_hi:[0,1]
	v_pk_mul_f32 v[100:101], v[80:81], v[4:5] op_sel:[1,0]
	v_pk_mul_f32 v[102:103], v[80:81], v[6:7] op_sel:[1,0]
	v_pk_fma_f32 v[96:97], v[82:83], v[8:9], v[96:97] op_sel_hi:[0,1,1]
	v_pk_fma_f32 v[98:99], v[82:83], v[10:11], v[98:99] op_sel_hi:[0,1,1]
	v_pk_fma_f32 v[100:101], v[82:83], v[12:13], v[100:101] op_sel:[1,0,0]
	v_pk_fma_f32 v[102:103], v[82:83], v[14:15], v[102:103] op_sel:[1,0,0]
	v_pk_fma_f32 v[96:97], v[84:85], v[16:17], v[96:97] op_sel_hi:[0,1,1]
	v_pk_fma_f32 v[98:99], v[84:85], v[18:19], v[98:99] op_sel_hi:[0,1,1]
	v_pk_fma_f32 v[100:101], v[86:87], v[20:21], v[100:101] op_sel_hi:[0,1,1]
	v_pk_fma_f32 v[102:103], v[86:87], v[22:23], v[102:103] op_sel_hi:[0,1,1]
	v_pk_fma_f32 v[96:97], v[86:87], v[24:25], v[96:97] op_sel:[1,0,0]
	v_pk_fma_f32 v[98:99], v[86:87], v[26:27], v[98:99] op_sel:[1,0,0]
	v_pk_fma_f32 v[100:101], v[88:89], v[28:29], v[100:101] op_sel_hi:[0,1,1]
	v_pk_fma_f32 v[102:103], v[88:89], v[30:31], v[102:103] op_sel_hi:[0,1,1]
	v_pk_fma_f32 v[96:97], v[88:89], v[32:33], v[96:97] op_sel:[1,0,0]
	v_pk_fma_f32 v[98:99], v[88:89], v[34:35], v[98:99] op_sel:[1,0,0]
	v_pk_add_f32 v[96:97], v[96:97], v[100:101]
	v_pk_add_f32 v[98:99], v[98:99], v[102:103]
	s_nop 1
	v_permlane16_swap_b32_e32 v96, v97
	v_permlane16_swap_b32_e32 v98, v99
	v_add_f32_e32 v96, v96, v97
	v_add_f32_e32 v98, v98, v99
	s_nop 1
	v_permlane32_swap_b32_e32 v96, v98
	v_add_f32_e32 v96, v96, v98
	s_waitcnt vmcnt(2)
	v_add_f32_e32 v96, v96, v72
	v_max_f32_e32 v96, 0, v96
	ds_write_b32 v78, v96
	ds_read2_b32 v[80:81], v79 offset0:0 offset1:4
	ds_read2_b32 v[82:83], v79 offset0:8 offset1:12
	ds_read2_b32 v[84:85], v79 offset0:16 offset1:20
	ds_read2_b32 v[86:87], v79 offset0:24 offset1:28
	ds_read2_b32 v[88:89], v79 offset0:32 offset1:36
	ds_read2_b32 v[90:91], v79 offset0:40 offset1:44
	ds_read2_b32 v[92:93], v79 offset0:48 offset1:52
	ds_read2_b32 v[94:95], v79 offset0:56 offset1:60
	s_waitcnt lgkmcnt(0)
	v_cmp_neq_f32_e64 s[40:41], 0, v80
	v_cmp_neq_f32_e64 s[42:43], 0, v81
	v_cmp_neq_f32_e64 s[44:45], 0, v82
	v_cmp_neq_f32_e64 s[46:47], 0, v83
	v_cmp_neq_f32_e64 s[48:49], 0, v84
	v_cmp_neq_f32_e64 s[50:51], 0, v85
	v_cmp_neq_f32_e64 s[52:53], 0, v86
	v_cmp_neq_f32_e64 s[54:55], 0, v87
	v_cmp_neq_f32_e64 s[56:57], 0, v88
	v_cmp_neq_f32_e64 s[58:59], 0, v89
	v_cmp_neq_f32_e64 s[60:61], 0, v90
	v_cmp_neq_f32_e64 s[62:63], 0, v91
	v_cmp_neq_f32_e64 s[64:65], 0, v92
	v_cmp_neq_f32_e64 s[66:67], 0, v93
	v_cmp_neq_f32_e64 s[68:69], 0, v94
	v_cmp_neq_f32_e64 s[70:71], 0, v95
	s_mov_b64 exec, s[40:41]
	global_load_dwordx4 v[0:3], v74, s[18:19] nt
	s_mov_b64 exec, s[42:43]
	global_load_dwordx4 v[4:7], v74, s[18:19] offset:1024 nt
	s_mov_b64 exec, s[44:45]
	global_load_dwordx4 v[8:11], v74, s[18:19] offset:2048 nt
	s_mov_b64 exec, s[46:47]
	global_load_dwordx4 v[12:15], v74, s[18:19] offset:3072 nt
	s_add_u32 s18, s18, 0x1000
	s_addc_u32 s19, s19, 0
	s_mov_b64 exec, s[48:49]
	global_load_dwordx4 v[16:19], v74, s[18:19] nt
	s_mov_b64 exec, s[50:51]
	global_load_dwordx4 v[20:23], v74, s[18:19] offset:1024 nt
	s_mov_b64 exec, s[52:53]
	global_load_dwordx4 v[24:27], v74, s[18:19] offset:2048 nt
	s_mov_b64 exec, s[54:55]
	global_load_dwordx4 v[28:31], v74, s[18:19] offset:3072 nt
	s_add_u32 s18, s18, 0x1000
	s_addc_u32 s19, s19, 0
	s_mov_b64 exec, s[56:57]
	global_load_dwordx4 v[32:35], v74, s[18:19] nt
	s_mov_b64 exec, s[58:59]
	global_load_dwordx4 v[36:39], v74, s[18:19] offset:1024 nt
	s_mov_b64 exec, s[60:61]
	global_load_dwordx4 v[40:43], v74, s[18:19] offset:2048 nt
	s_mov_b64 exec, s[62:63]
	global_load_dwordx4 v[44:47], v74, s[18:19] offset:3072 nt
	s_add_u32 s18, s18, 0x1000
	s_addc_u32 s19, s19, 0
	s_mov_b64 exec, s[64:65]
	global_load_dwordx4 v[48:51], v74, s[18:19] nt
	s_mov_b64 exec, s[66:67]
	global_load_dwordx4 v[52:55], v74, s[18:19] offset:1024 nt
	s_mov_b64 exec, s[68:69]
	global_load_dwordx4 v[56:59], v74, s[18:19] offset:2048 nt
	s_mov_b64 exec, s[70:71]
	global_load_dwordx4 v[60:63], v74, s[18:19] offset:3072 nt
	s_mov_b64 exec, -1
	v_mov_b32_e32 v96, 0
	v_mov_b32_e32 v97, 0
	v_mov_b32_e32 v98, 0
	v_mov_b32_e32 v99, 0
	v_mov_b32_e32 v100, 0
	v_mov_b32_e32 v101, 0
	v_mov_b32_e32 v102, 0
	v_mov_b32_e32 v103, 0
	s_waitcnt vmcnt(0)
	s_mov_b64 exec, s[40:41]
	v_pk_fma_f32 v[96:97], v[80:81], v[0:1], v[96:97] op_sel_hi:[0,1,1]
	v_pk_fma_f32 v[98:99], v[80:81], v[2:3], v[98:99] op_sel_hi:[0,1,1]
	s_mov_b64 exec, s[42:43]
	v_pk_fma_f32 v[100:101], v[80:81], v[4:5], v[100:101] op_sel:[1,0,0]
	v_pk_fma_f32 v[102:103], v[80:81], v[6:7], v[102:103] op_sel:[1,0,0]
	s_mov_b64 exec, s[44:45]
	v_pk_fma_f32 v[96:97], v[82:83], v[8:9], v[96:97] op_sel_hi:[0,1,1]
	v_pk_fma_f32 v[98:99], v[82:83], v[10:11], v[98:99] op_sel_hi:[0,1,1]
	s_mov_b64 exec, s[46:47]
	v_pk_fma_f32 v[100:101], v[82:83], v[12:13], v[100:101] op_sel:[1,0,0]
	v_pk_fma_f32 v[102:103], v[82:83], v[14:15], v[102:103] op_sel:[1,0,0]
	s_mov_b64 exec, s[48:49]
	v_pk_fma_f32 v[96:97], v[84:85], v[16:17], v[96:97] op_sel_hi:[0,1,1]
	v_pk_fma_f32 v[98:99], v[84:85], v[18:19], v[98:99] op_sel_hi:[0,1,1]
	s_mov_b64 exec, s[50:51]
	v_pk_fma_f32 v[100:101], v[84:85], v[20:21], v[100:101] op_sel:[1,0,0]
	v_pk_fma_f32 v[102:103], v[84:85], v[22:23], v[102:103] op_sel:[1,0,0]
	s_mov_b64 exec, s[52:53]
	v_pk_fma_f32 v[96:97], v[86:87], v[24:25], v[96:97] op_sel_hi:[0,1,1]
	v_pk_fma_f32 v[98:99], v[86:87], v[26:27], v[98:99] op_sel_hi:[0,1,1]
	s_mov_b64 exec, s[54:55]
	v_pk_fma_f32 v[100:101], v[86:87], v[28:29], v[100:101] op_sel:[1,0,0]
	v_pk_fma_f32 v[102:103], v[86:87], v[30:31], v[102:103] op_sel:[1,0,0]
	s_mov_b64 exec, s[56:57]
	v_pk_fma_f32 v[96:97], v[88:89], v[32:33], v[96:97] op_sel_hi:[0,1,1]
	v_pk_fma_f32 v[98:99], v[88:89], v[34:35], v[98:99] op_sel_hi:[0,1,1]
	s_mov_b64 exec, s[58:59]
	v_pk_fma_f32 v[100:101], v[88:89], v[36:37], v[100:101] op_sel:[1,0,0]
	v_pk_fma_f32 v[102:103], v[88:89], v[38:39], v[102:103] op_sel:[1,0,0]
	s_mov_b64 exec, s[60:61]
	v_pk_fma_f32 v[96:97], v[90:91], v[40:41], v[96:97] op_sel_hi:[0,1,1]
	v_pk_fma_f32 v[98:99], v[90:91], v[42:43], v[98:99] op_sel_hi:[0,1,1]
	s_mov_b64 exec, s[62:63]
	v_pk_fma_f32 v[100:101], v[90:91], v[44:45], v[100:101] op_sel:[1,0,0]
	v_pk_fma_f32 v[102:103], v[90:91], v[46:47], v[102:103] op_sel:[1,0,0]
	s_mov_b64 exec, s[64:65]
	v_pk_fma_f32 v[96:97], v[92:93], v[48:49], v[96:97] op_sel_hi:[0,1,1]
	v_pk_fma_f32 v[98:99], v[92:93], v[50:51], v[98:99] op_sel_hi:[0,1,1]
	s_mov_b64 exec, s[66:67]
	v_pk_fma_f32 v[100:101], v[92:93], v[52:53], v[100:101] op_sel:[1,0,0]
	v_pk_fma_f32 v[102:103], v[92:93], v[54:55], v[102:103] op_sel:[1,0,0]
	s_mov_b64 exec, s[68:69]
	v_pk_fma_f32 v[96:97], v[94:95], v[56:57], v[96:97] op_sel_hi:[0,1,1]
	v_pk_fma_f32 v[98:99], v[94:95], v[58:59], v[98:99] op_sel_hi:[0,1,1]
	s_mov_b64 exec, s[70:71]
	v_pk_fma_f32 v[100:101], v[94:95], v[60:61], v[100:101] op_sel:[1,0,0]
	v_pk_fma_f32 v[102:103], v[94:95], v[62:63], v[102:103] op_sel:[1,0,0]
	s_mov_b64 exec, -1
	ds_read_b128 v[0:3], v74
	ds_read_b128 v[4:7], v74 offset:1024
	ds_read_b128 v[8:11], v74 offset:2048
	ds_read_b128 v[12:15], v74 offset:3072
	ds_read_b128 v[16:19], v74 offset:4096
	ds_read_b128 v[20:23], v74 offset:5120
	ds_read_b128 v[24:27], v74 offset:6144
	ds_read_b128 v[28:31], v74 offset:7168
	ds_read_b128 v[32:35], v74 offset:8192
	ds_read_b128 v[36:39], v74 offset:9216
	ds_read_b128 v[40:43], v74 offset:10240
	ds_read_b128 v[44:47], v74 offset:11264
	ds_read_b128 v[48:51], v74 offset:12288
	ds_read_b128 v[52:55], v74 offset:13312
	ds_read_b128 v[56:59], v74 offset:14336
	v_pk_add_f32 v[96:97], v[96:97], v[100:101]
	v_pk_add_f32 v[98:99], v[98:99], v[102:103]
	s_nop 1
	v_permlane16_swap_b32_e32 v96, v97
	v_permlane16_swap_b32_e32 v98, v99
	v_add_f32_e32 v96, v96, v97
	v_add_f32_e32 v98, v98, v99
	s_nop 1
	v_permlane32_swap_b32_e32 v96, v98
	v_add_f32_e32 v96, v96, v98
	v_add_f32_e32 v96, v96, v64
	s_waitcnt lgkmcnt(5)
	ds_read_b128 v[60:63], v74 offset:15360
	ds_write_b32 v78, v96
	ds_read2_b32 v[80:81], v79 offset0:0 offset1:4
	ds_read2_b32 v[82:83], v79 offset0:8 offset1:12
	ds_read2_b32 v[84:85], v79 offset0:16 offset1:20
	ds_read2_b32 v[86:87], v79 offset0:24 offset1:28
	ds_read2_b32 v[88:89], v79 offset0:32 offset1:36
	ds_read2_b32 v[90:91], v79 offset0:40 offset1:44
	ds_read2_b32 v[92:93], v79 offset0:48 offset1:52
	ds_read2_b32 v[94:95], v79 offset0:56 offset1:60
	v_lshlrev_b32_e32 v72, 3, v76
	v_lshl_or_b32 v72, v75, 2, v72
	v_cmp_gt_u32_e32 vcc, 2, v75
	s_waitcnt lgkmcnt(0)
	v_pk_mul_f32 v[96:97], v[80:81], v[0:1] op_sel_hi:[0,1]
	v_pk_mul_f32 v[98:99], v[80:81], v[2:3] op_sel_hi:[0,1]
	v_pk_mul_f32 v[100:101], v[80:81], v[4:5] op_sel:[1,0]
	v_pk_mul_f32 v[102:103], v[80:81], v[6:7] op_sel:[1,0]
	v_pk_fma_f32 v[96:97], v[82:83], v[8:9], v[96:97] op_sel_hi:[0,1,1]
	v_pk_fma_f32 v[98:99], v[82:83], v[10:11], v[98:99] op_sel_hi:[0,1,1]
	v_pk_fma_f32 v[100:101], v[82:83], v[12:13], v[100:101] op_sel:[1,0,0]
	v_pk_fma_f32 v[102:103], v[82:83], v[14:15], v[102:103] op_sel:[1,0,0]
	v_pk_fma_f32 v[96:97], v[84:85], v[16:17], v[96:97] op_sel_hi:[0,1,1]
	v_pk_fma_f32 v[98:99], v[84:85], v[18:19], v[98:99] op_sel_hi:[0,1,1]
	v_pk_fma_f32 v[100:101], v[84:85], v[20:21], v[100:101] op_sel:[1,0,0]
	v_pk_fma_f32 v[102:103], v[84:85], v[22:23], v[102:103] op_sel:[1,0,0]
	v_pk_fma_f32 v[96:97], v[86:87], v[24:25], v[96:97] op_sel_hi:[0,1,1]
	v_pk_fma_f32 v[98:99], v[86:87], v[26:27], v[98:99] op_sel_hi:[0,1,1]
	v_pk_fma_f32 v[100:101], v[86:87], v[28:29], v[100:101] op_sel:[1,0,0]
	v_pk_fma_f32 v[102:103], v[86:87], v[30:31], v[102:103] op_sel:[1,0,0]
	v_pk_fma_f32 v[96:97], v[88:89], v[32:33], v[96:97] op_sel_hi:[0,1,1]
	v_pk_fma_f32 v[98:99], v[88:89], v[34:35], v[98:99] op_sel_hi:[0,1,1]
	v_pk_fma_f32 v[100:101], v[88:89], v[36:37], v[100:101] op_sel:[1,0,0]
	v_pk_fma_f32 v[102:103], v[88:89], v[38:39], v[102:103] op_sel:[1,0,0]
	v_pk_fma_f32 v[96:97], v[90:91], v[40:41], v[96:97] op_sel_hi:[0,1,1]
	v_pk_fma_f32 v[98:99], v[90:91], v[42:43], v[98:99] op_sel_hi:[0,1,1]
	v_pk_fma_f32 v[100:101], v[90:91], v[44:45], v[100:101] op_sel:[1,0,0]
	v_pk_fma_f32 v[102:103], v[90:91], v[46:47], v[102:103] op_sel:[1,0,0]
	v_pk_fma_f32 v[96:97], v[92:93], v[48:49], v[96:97] op_sel_hi:[0,1,1]
	v_pk_fma_f32 v[98:99], v[92:93], v[50:51], v[98:99] op_sel_hi:[0,1,1]
	v_pk_fma_f32 v[100:101], v[92:93], v[52:53], v[100:101] op_sel:[1,0,0]
	v_pk_fma_f32 v[102:103], v[92:93], v[54:55], v[102:103] op_sel:[1,0,0]
	v_pk_fma_f32 v[96:97], v[94:95], v[56:57], v[96:97] op_sel_hi:[0,1,1]
	v_pk_fma_f32 v[98:99], v[94:95], v[58:59], v[98:99] op_sel_hi:[0,1,1]
	v_pk_fma_f32 v[100:101], v[94:95], v[60:61], v[100:101] op_sel:[1,0,0]
	v_pk_fma_f32 v[102:103], v[94:95], v[62:63], v[102:103] op_sel:[1,0,0]
	v_pk_add_f32 v[96:97], v[96:97], v[100:101]
	v_pk_add_f32 v[98:99], v[98:99], v[102:103]
	s_nop 1
	v_permlane16_swap_b32_e32 v96, v98
	v_permlane16_swap_b32_e32 v97, v99
	v_add_f32_e32 v96, v96, v98
	v_add_f32_e32 v97, v97, v99
	v_mov_b32_e32 v80, v96
	v_mov_b32_e32 v81, v97
	s_nop 1
	v_permlane32_swap_b32_e32 v96, v80
	v_permlane32_swap_b32_e32 v97, v81
	v_add_f32_e32 v96, v96, v80
	v_add_f32_e32 v97, v97, v81
	v_cvt_pk_f16_f32 v73, v96, v97
	s_and_saveexec_b64 s[4:5], vcc
	global_atomic_pk_add_f16 v72, v73, s[24:25]
	s_endpgm
	.p2align	8

_Z11edge_kernelILi64ELb0EEvPKfS1_PKDF16_PKiS5_S1_S1_S1_S1_S1_PDF16_:
	s_load_dwordx16 s[4:19], s[0:1], 0x10
	s_load_dwordx2 s[20:21], s[0:1], 0x50
	v_readfirstlane_b32 s3, v0
	v_bfe_u32 v75, v0, 4, 2
	v_and_b32_e32 v76, 15, v0
	v_and_b32_e32 v78, 63, v0
	s_lshr_b32 s3, s3, 6
	s_lshl_b32 s2, s2, 1
	s_add_i32 s2, s2, s3
	v_lshlrev_b32_e32 v74, 8, v75
	v_lshl_or_b32 v74, v76, 4, v74
	v_lshlrev_b32_e32 v79, 4, v78
	v_lshl_or_b32 v77, v76, 2, v75
	v_lshlrev_b32_e32 v77, 2, v77
	v_lshlrev_b32_e32 v78, 5, v75
	v_lshlrev_b32_e32 v73, 12, v75
	v_lshl_or_b32 v73, v76, 4, v73
	s_lshl_b32 s28, s2, 14
	s_lshl_b32 s29, s2, 14
	s_lshl_b32 s30, s2, 2
	s_lshl_b32 s31, s2, 8
	s_lshl_b32 s33, s3, 10
	s_lshl_b32 s34, s3, 8
	s_addk_i32 s34, 0x4000
	s_waitcnt lgkmcnt(0)
	s_add_u32 s6, s6, s30
	s_addc_u32 s7, s7, 0
	s_add_u32 s8, s8, s30
	s_addc_u32 s9, s9, 0
	s_load_dword s35, s[6:7], 0x0
	s_load_dword s36, s[8:9], 0x0
	s_add_u32 s10, s10, s28
	s_addc_u32 s11, s11, 0
	s_add_u32 s18, s18, s33
	s_addc_u32 s19, s19, 0
	s_add_u32 s14, s14, s29
	s_addc_u32 s15, s15, 0
	s_add_u32 s12, s12, s31
	s_addc_u32 s13, s13, 0
	s_add_u32 s16, s16, s31
	s_addc_u32 s17, s17, 0
	s_waitcnt lgkmcnt(0)
	s_lshl_b32 s36, s36, 7
	s_add_u32 s20, s20, s36
	s_addc_u32 s21, s21, 0
	s_lshl_b32 s37, s35, 7
	s_add_u32 s4, s4, s37
	s_addc_u32 s5, s5, 0
	global_load_dwordx4 v[64:67], v78, s[4:5] nt
	global_load_dwordx4 v[68:71], v78, s[4:5] offset:16 nt
	v_add_u32_e32 v78, s34, v77
	s_waitcnt vmcnt(0)
	v_cvt_f32_f16_e32 v80, v64
	v_cvt_f32_f16_sdwa v81, v64 dst_sel:DWORD dst_unused:UNUSED_PAD src0_sel:WORD_1
	v_cvt_f32_f16_e32 v82, v65
	v_cvt_f32_f16_sdwa v83, v65 dst_sel:DWORD dst_unused:UNUSED_PAD src0_sel:WORD_1
	v_cvt_f32_f16_e32 v84, v66
	v_cvt_f32_f16_sdwa v85, v66 dst_sel:DWORD dst_unused:UNUSED_PAD src0_sel:WORD_1
	v_cvt_f32_f16_e32 v86, v67
	v_cvt_f32_f16_sdwa v87, v67 dst_sel:DWORD dst_unused:UNUSED_PAD src0_sel:WORD_1
	v_cvt_f32_f16_e32 v88, v68
	v_cvt_f32_f16_sdwa v89, v68 dst_sel:DWORD dst_unused:UNUSED_PAD src0_sel:WORD_1
	v_cvt_f32_f16_e32 v90, v69
	v_cvt_f32_f16_sdwa v91, v69 dst_sel:DWORD dst_unused:UNUSED_PAD src0_sel:WORD_1
	v_cvt_f32_f16_e32 v92, v70
	v_cvt_f32_f16_sdwa v93, v70 dst_sel:DWORD dst_unused:UNUSED_PAD src0_sel:WORD_1
	v_cvt_f32_f16_e32 v94, v71
	v_cvt_f32_f16_sdwa v95, v71 dst_sel:DWORD dst_unused:UNUSED_PAD src0_sel:WORD_1
	v_max_f32_e32 v80, 0, v80
	v_max_f32_e32 v81, 0, v81
	v_max_f32_e32 v82, 0, v82
	v_max_f32_e32 v83, 0, v83
	v_max_f32_e32 v84, 0, v84
	v_max_f32_e32 v85, 0, v85
	v_max_f32_e32 v86, 0, v86
	v_max_f32_e32 v87, 0, v87
	v_max_f32_e32 v88, 0, v88
	v_max_f32_e32 v89, 0, v89
	v_max_f32_e32 v90, 0, v90
	v_max_f32_e32 v91, 0, v91
	v_max_f32_e32 v92, 0, v92
	v_max_f32_e32 v93, 0, v93
	v_max_f32_e32 v94, 0, v94
	v_max_f32_e32 v95, 0, v95
	v_cmp_neq_f32_e64 s[40:41], 0, v80
	v_cmp_neq_f32_e64 s[42:43], 0, v81
	v_cmp_neq_f32_e64 s[44:45], 0, v82
	v_cmp_neq_f32_e64 s[46:47], 0, v83
	v_cmp_neq_f32_e64 s[48:49], 0, v84
	v_cmp_neq_f32_e64 s[50:51], 0, v85
	v_cmp_neq_f32_e64 s[52:53], 0, v86
	v_cmp_neq_f32_e64 s[54:55], 0, v87
	v_cmp_neq_f32_e64 s[56:57], 0, v88
	v_cmp_neq_f32_e64 s[58:59], 0, v89
	v_cmp_neq_f32_e64 s[60:61], 0, v90
	v_cmp_neq_f32_e64 s[62:63], 0, v91
	v_cmp_neq_f32_e64 s[64:65], 0, v92
	v_cmp_neq_f32_e64 s[66:67], 0, v93
	v_cmp_neq_f32_e64 s[68:69], 0, v94
	v_cmp_neq_f32_e64 s[70:71], 0, v95
	v_lshlrev_b32_e32 v96, 12, v75
	v_lshl_or_b32 v96, v76, 4, v96
	s_mov_b64 exec, s[40:41]
	global_load_dwordx4 v[0:3], v96, s[10:11] nt
	s_mov_b64 exec, s[42:43]
	global_load_dwordx4 v[4:7], v96, s[10:11] offset:256 nt
	s_mov_b64 exec, s[44:45]
	global_load_dwordx4 v[8:11], v96, s[10:11] offset:512 nt
	s_mov_b64 exec, s[46:47]
	global_load_dwordx4 v[12:15], v96, s[10:11] offset:768 nt
	s_mov_b64 exec, s[48:49]
	global_load_dwordx4 v[16:19], v96, s[10:11] offset:1024 nt
	s_mov_b64 exec, s[50:51]
	global_load_dwordx4 v[20:23], v96, s[10:11] offset:1280 nt
	s_mov_b64 exec, s[52:53]
	global_load_dwordx4 v[24:27], v96, s[10:11] offset:1536 nt
	s_mov_b64 exec, s[54:55]
	global_load_dwordx4 v[28:31], v96, s[10:11] offset:1792 nt
	s_mov_b64 exec, s[56:57]
	global_load_dwordx4 v[32:35], v96, s[10:11] offset:2048 nt
	s_mov_b64 exec, s[58:59]
	global_load_dwordx4 v[36:39], v96, s[10:11] offset:2304 nt
	s_mov_b64 exec, s[60:61]
	global_load_dwordx4 v[40:43], v96, s[10:11] offset:2560 nt
	s_mov_b64 exec, s[62:63]
	global_load_dwordx4 v[44:47], v96, s[10:11] offset:2816 nt
	s_mov_b64 exec, s[64:65]
	global_load_dwordx4 v[48:51], v96, s[10:11] offset:3072 nt
	s_mov_b64 exec, s[66:67]
	global_load_dwordx4 v[52:55], v96, s[10:11] offset:3328 nt
	s_mov_b64 exec, s[68:69]
	global_load_dwordx4 v[56:59], v96, s[10:11] offset:3584 nt
	s_mov_b64 exec, s[70:71]
	global_load_dwordx4 v[60:63], v96, s[10:11] offset:3840 nt
	s_mov_b64 exec, -1
	s_mov_b32 m0, s33
	s_nop 0
	global_load_lds_dwordx4 v79, s[18:19]
	global_load_lds_dwordx4 v79, s[18:19] offset:2048
	s_add_u32 m0, m0, 0x1000
	s_add_u32 s18, s18, 0x1000
	s_addc_u32 s19, s19, 0
	global_load_lds_dwordx4 v79, s[18:19]
	global_load_lds_dwordx4 v79, s[18:19] offset:2048
	s_add_u32 m0, m0, 0x1000
	s_add_u32 s18, s18, 0x1000
	s_addc_u32 s19, s19, 0
	global_load_lds_dwordx4 v79, s[18:19]
	global_load_lds_dwordx4 v79, s[18:19] offset:2048
	s_add_u32 m0, m0, 0x1000
	s_add_u32 s18, s18, 0x1000
	s_addc_u32 s19, s19, 0
	global_load_lds_dwordx4 v79, s[18:19]
	global_load_lds_dwordx4 v79, s[18:19] offset:2048
	global_load_dword v72, v77, s[12:13] nt
	v_mov_b32_e32 v65, 0
	global_load_dword v73, v77, s[16:17] nt
	global_load_dword v64, v65, s[20:21]
	v_lshl_add_u32 v79, v75, 2, s34
	v_mov_b32_e32 v96, 0
	v_mov_b32_e32 v97, 0
	v_mov_b32_e32 v98, 0
	v_mov_b32_e32 v99, 0
	v_mov_b32_e32 v100, 0
	v_mov_b32_e32 v101, 0
	v_mov_b32_e32 v102, 0
	v_mov_b32_e32 v103, 0
	s_waitcnt vmcnt(0)
	s_barrier
	s_mov_b64 exec, s[40:41]
	v_pk_fma_f32 v[96:97], v[80:81], v[0:1], v[96:97] op_sel_hi:[0,1,1]
	v_pk_fma_f32 v[98:99], v[80:81], v[2:3], v[98:99] op_sel_hi:[0,1,1]
	s_mov_b64 exec, s[42:43]
	v_pk_fma_f32 v[100:101], v[80:81], v[4:5], v[100:101] op_sel:[1,0,0]
	v_pk_fma_f32 v[102:103], v[80:81], v[6:7], v[102:103] op_sel:[1,0,0]
	s_mov_b64 exec, s[44:45]
	v_pk_fma_f32 v[96:97], v[82:83], v[8:9], v[96:97] op_sel_hi:[0,1,1]
	v_pk_fma_f32 v[98:99], v[82:83], v[10:11], v[98:99] op_sel_hi:[0,1,1]
	s_mov_b64 exec, s[46:47]
	v_pk_fma_f32 v[100:101], v[82:83], v[12:13], v[100:101] op_sel:[1,0,0]
	v_pk_fma_f32 v[102:103], v[82:83], v[14:15], v[102:103] op_sel:[1,0,0]
	s_mov_b64 exec, s[48:49]
	v_pk_fma_f32 v[96:97], v[84:85], v[16:17], v[96:97] op_sel_hi:[0,1,1]
	v_pk_fma_f32 v[98:99], v[84:85], v[18:19], v[98:99] op_sel_hi:[0,1,1]
	s_mov_b64 exec, s[50:51]
	v_pk_fma_f32 v[100:101], v[84:85], v[20:21], v[100:101] op_sel:[1,0,0]
	v_pk_fma_f32 v[102:103], v[84:85], v[22:23], v[102:103] op_sel:[1,0,0]
	s_mov_b64 exec, s[52:53]
	v_pk_fma_f32 v[96:97], v[86:87], v[24:25], v[96:97] op_sel_hi:[0,1,1]
	v_pk_fma_f32 v[98:99], v[86:87], v[26:27], v[98:99] op_sel_hi:[0,1,1]
	s_mov_b64 exec, s[54:55]
	v_pk_fma_f32 v[100:101], v[86:87], v[28:29], v[100:101] op_sel:[1,0,0]
	v_pk_fma_f32 v[102:103], v[86:87], v[30:31], v[102:103] op_sel:[1,0,0]
	s_mov_b64 exec, s[56:57]
	v_pk_fma_f32 v[96:97], v[88:89], v[32:33], v[96:97] op_sel_hi:[0,1,1]
	v_pk_fma_f32 v[98:99], v[88:89], v[34:35], v[98:99] op_sel_hi:[0,1,1]
	s_mov_b64 exec, s[58:59]
	v_pk_fma_f32 v[100:101], v[88:89], v[36:37], v[100:101] op_sel:[1,0,0]
	v_pk_fma_f32 v[102:103], v[88:89], v[38:39], v[102:103] op_sel:[1,0,0]
	s_mov_b64 exec, s[60:61]
	v_pk_fma_f32 v[96:97], v[90:91], v[40:41], v[96:97] op_sel_hi:[0,1,1]
	v_pk_fma_f32 v[98:99], v[90:91], v[42:43], v[98:99] op_sel_hi:[0,1,1]
	s_mov_b64 exec, s[62:63]
	v_pk_fma_f32 v[100:101], v[90:91], v[44:45], v[100:101] op_sel:[1,0,0]
	v_pk_fma_f32 v[102:103], v[90:91], v[46:47], v[102:103] op_sel:[1,0,0]
	s_mov_b64 exec, s[64:65]
	v_pk_fma_f32 v[96:97], v[92:93], v[48:49], v[96:97] op_sel_hi:[0,1,1]
	v_pk_fma_f32 v[98:99], v[92:93], v[50:51], v[98:99] op_sel_hi:[0,1,1]
	s_mov_b64 exec, s[66:67]
	v_pk_fma_f32 v[100:101], v[92:93], v[52:53], v[100:101] op_sel:[1,0,0]
	v_pk_fma_f32 v[102:103], v[92:93], v[54:55], v[102:103] op_sel:[1,0,0]
	s_mov_b64 exec, s[68:69]
	v_pk_fma_f32 v[96:97], v[94:95], v[56:57], v[96:97] op_sel_hi:[0,1,1]
	v_pk_fma_f32 v[98:99], v[94:95], v[58:59], v[98:99] op_sel_hi:[0,1,1]
	s_mov_b64 exec, s[70:71]
	v_pk_fma_f32 v[100:101], v[94:95], v[60:61], v[100:101] op_sel:[1,0,0]
	v_pk_fma_f32 v[102:103], v[94:95], v[62:63], v[102:103] op_sel:[1,0,0]
	s_mov_b64 exec, -1
	v_pk_add_f32 v[96:97], v[96:97], v[100:101]
	v_pk_add_f32 v[98:99], v[98:99], v[102:103]
	s_nop 1
	v_permlane16_swap_b32_e32 v96, v97
	v_permlane16_swap_b32_e32 v98, v99
	v_add_f32_e32 v96, v96, v97
	v_add_f32_e32 v98, v98, v99
	s_nop 1
	v_permlane32_swap_b32_e32 v96, v98
	v_add_f32_e32 v96, v96, v98
	s_waitcnt vmcnt(1)
	v_add_f32_e32 v96, v96, v72
	v_max_f32_e32 v96, 0, v96
	ds_write_b32 v78, v96
	ds_read2_b32 v[80:81], v79 offset0:0 offset1:4
	ds_read2_b32 v[82:83], v79 offset0:8 offset1:12
	ds_read2_b32 v[84:85], v79 offset0:16 offset1:20
	ds_read2_b32 v[86:87], v79 offset0:24 offset1:28
	ds_read2_b32 v[88:89], v79 offset0:32 offset1:36
	ds_read2_b32 v[90:91], v79 offset0:40 offset1:44
	ds_read2_b32 v[92:93], v79 offset0:48 offset1:52
	ds_read2_b32 v[94:95], v79 offset0:56 offset1:60
	s_waitcnt lgkmcnt(0)
	v_cmp_neq_f32_e64 s[40:41], 0, v80
	v_cmp_neq_f32_e64 s[42:43], 0, v81
	v_cmp_neq_f32_e64 s[44:45], 0, v82
	v_cmp_neq_f32_e64 s[46:47], 0, v83
	v_cmp_neq_f32_e64 s[48:49], 0, v84
	v_cmp_neq_f32_e64 s[50:51], 0, v85
	v_cmp_neq_f32_e64 s[52:53], 0, v86
	v_cmp_neq_f32_e64 s[54:55], 0, v87
	v_cmp_neq_f32_e64 s[56:57], 0, v88
	v_cmp_neq_f32_e64 s[58:59], 0, v89
	v_cmp_neq_f32_e64 s[60:61], 0, v90
	v_cmp_neq_f32_e64 s[62:63], 0, v91
	v_cmp_neq_f32_e64 s[64:65], 0, v92
	v_cmp_neq_f32_e64 s[66:67], 0, v93
	v_cmp_neq_f32_e64 s[68:69], 0, v94
	v_cmp_neq_f32_e64 s[70:71], 0, v95
	s_mov_b64 exec, s[40:41]
	global_load_dwordx4 v[0:3], v74, s[14:15] nt
	s_mov_b64 exec, s[42:43]
	global_load_dwordx4 v[4:7], v74, s[14:15] offset:1024 nt
	s_mov_b64 exec, s[44:45]
	global_load_dwordx4 v[8:11], v74, s[14:15] offset:2048 nt
	s_mov_b64 exec, s[46:47]
	global_load_dwordx4 v[12:15], v74, s[14:15] offset:3072 nt
	s_add_u32 s14, s14, 0x1000
	s_addc_u32 s15, s15, 0
	s_mov_b64 exec, s[48:49]
	global_load_dwordx4 v[16:19], v74, s[14:15] nt
	s_mov_b64 exec, s[50:51]
	global_load_dwordx4 v[20:23], v74, s[14:15] offset:1024 nt
	s_mov_b64 exec, s[52:53]
	global_load_dwordx4 v[24:27], v74, s[14:15] offset:2048 nt
	s_mov_b64 exec, s[54:55]
	global_load_dwordx4 v[28:31], v74, s[14:15] offset:3072 nt
	s_add_u32 s14, s14, 0x1000
	s_addc_u32 s15, s15, 0
	s_mov_b64 exec, s[56:57]
	global_load_dwordx4 v[32:35], v74, s[14:15] nt
	s_mov_b64 exec, s[58:59]
	global_load_dwordx4 v[36:39], v74, s[14:15] offset:1024 nt
	s_mov_b64 exec, s[60:61]
	global_load_dwordx4 v[40:43], v74, s[14:15] offset:2048 nt
	s_mov_b64 exec, s[62:63]
	global_load_dwordx4 v[44:47], v74, s[14:15] offset:3072 nt
	s_add_u32 s14, s14, 0x1000
	s_addc_u32 s15, s15, 0
	s_mov_b64 exec, s[64:65]
	global_load_dwordx4 v[48:51], v74, s[14:15] nt
	s_mov_b64 exec, s[66:67]
	global_load_dwordx4 v[52:55], v74, s[14:15] offset:1024 nt
	s_mov_b64 exec, s[68:69]
	global_load_dwordx4 v[56:59], v74, s[14:15] offset:2048 nt
	s_mov_b64 exec, s[70:71]
	global_load_dwordx4 v[60:63], v74, s[14:15] offset:3072 nt
	s_mov_b64 exec, -1
	v_mov_b32_e32 v96, 0
	v_mov_b32_e32 v97, 0
	v_mov_b32_e32 v98, 0
	v_mov_b32_e32 v99, 0
	v_mov_b32_e32 v100, 0
	v_mov_b32_e32 v101, 0
	v_mov_b32_e32 v102, 0
	v_mov_b32_e32 v103, 0
	s_waitcnt vmcnt(0)
	s_mov_b64 exec, s[40:41]
	v_pk_fma_f32 v[96:97], v[80:81], v[0:1], v[96:97] op_sel_hi:[0,1,1]
	v_pk_fma_f32 v[98:99], v[80:81], v[2:3], v[98:99] op_sel_hi:[0,1,1]
	s_mov_b64 exec, s[42:43]
	v_pk_fma_f32 v[100:101], v[80:81], v[4:5], v[100:101] op_sel:[1,0,0]
	v_pk_fma_f32 v[102:103], v[80:81], v[6:7], v[102:103] op_sel:[1,0,0]
	s_mov_b64 exec, s[44:45]
	v_pk_fma_f32 v[96:97], v[82:83], v[8:9], v[96:97] op_sel_hi:[0,1,1]
	v_pk_fma_f32 v[98:99], v[82:83], v[10:11], v[98:99] op_sel_hi:[0,1,1]
	s_mov_b64 exec, s[46:47]
	v_pk_fma_f32 v[100:101], v[82:83], v[12:13], v[100:101] op_sel:[1,0,0]
	v_pk_fma_f32 v[102:103], v[82:83], v[14:15], v[102:103] op_sel:[1,0,0]
	s_mov_b64 exec, s[48:49]
	v_pk_fma_f32 v[96:97], v[84:85], v[16:17], v[96:97] op_sel_hi:[0,1,1]
	v_pk_fma_f32 v[98:99], v[84:85], v[18:19], v[98:99] op_sel_hi:[0,1,1]
	s_mov_b64 exec, s[50:51]
	v_pk_fma_f32 v[100:101], v[84:85], v[20:21], v[100:101] op_sel:[1,0,0]
	v_pk_fma_f32 v[102:103], v[84:85], v[22:23], v[102:103] op_sel:[1,0,0]
	s_mov_b64 exec, s[52:53]
	v_pk_fma_f32 v[96:97], v[86:87], v[24:25], v[96:97] op_sel_hi:[0,1,1]
	v_pk_fma_f32 v[98:99], v[86:87], v[26:27], v[98:99] op_sel_hi:[0,1,1]
	s_mov_b64 exec, s[54:55]
	v_pk_fma_f32 v[100:101], v[86:87], v[28:29], v[100:101] op_sel:[1,0,0]
	v_pk_fma_f32 v[102:103], v[86:87], v[30:31], v[102:103] op_sel:[1,0,0]
	s_mov_b64 exec, s[56:57]
	v_pk_fma_f32 v[96:97], v[88:89], v[32:33], v[96:97] op_sel_hi:[0,1,1]
	v_pk_fma_f32 v[98:99], v[88:89], v[34:35], v[98:99] op_sel_hi:[0,1,1]
	s_mov_b64 exec, s[58:59]
	v_pk_fma_f32 v[100:101], v[88:89], v[36:37], v[100:101] op_sel:[1,0,0]
	v_pk_fma_f32 v[102:103], v[88:89], v[38:39], v[102:103] op_sel:[1,0,0]
	s_mov_b64 exec, s[60:61]
	v_pk_fma_f32 v[96:97], v[90:91], v[40:41], v[96:97] op_sel_hi:[0,1,1]
	v_pk_fma_f32 v[98:99], v[90:91], v[42:43], v[98:99] op_sel_hi:[0,1,1]
	s_mov_b64 exec, s[62:63]
	v_pk_fma_f32 v[100:101], v[90:91], v[44:45], v[100:101] op_sel:[1,0,0]
	v_pk_fma_f32 v[102:103], v[90:91], v[46:47], v[102:103] op_sel:[1,0,0]
	s_mov_b64 exec, s[64:65]
	v_pk_fma_f32 v[96:97], v[92:93], v[48:49], v[96:97] op_sel_hi:[0,1,1]
	v_pk_fma_f32 v[98:99], v[92:93], v[50:51], v[98:99] op_sel_hi:[0,1,1]
	s_mov_b64 exec, s[66:67]
	v_pk_fma_f32 v[100:101], v[92:93], v[52:53], v[100:101] op_sel:[1,0,0]
	v_pk_fma_f32 v[102:103], v[92:93], v[54:55], v[102:103] op_sel:[1,0,0]
	s_mov_b64 exec, s[68:69]
	v_pk_fma_f32 v[96:97], v[94:95], v[56:57], v[96:97] op_sel_hi:[0,1,1]
	v_pk_fma_f32 v[98:99], v[94:95], v[58:59], v[98:99] op_sel_hi:[0,1,1]
	s_mov_b64 exec, s[70:71]
	v_pk_fma_f32 v[100:101], v[94:95], v[60:61], v[100:101] op_sel:[1,0,0]
	v_pk_fma_f32 v[102:103], v[94:95], v[62:63], v[102:103] op_sel:[1,0,0]
	s_mov_b64 exec, -1
	ds_read_b128 v[0:3], v74
	ds_read_b128 v[4:7], v74 offset:1024
	ds_read_b128 v[8:11], v74 offset:2048
	ds_read_b128 v[12:15], v74 offset:3072
	ds_read_b128 v[16:19], v74 offset:4096
	ds_read_b128 v[20:23], v74 offset:5120
	ds_read_b128 v[24:27], v74 offset:6144
	ds_read_b128 v[28:31], v74 offset:7168
	ds_read_b128 v[32:35], v74 offset:8192
	ds_read_b128 v[36:39], v74 offset:9216
	ds_read_b128 v[40:43], v74 offset:10240
	ds_read_b128 v[44:47], v74 offset:11264
	ds_read_b128 v[48:51], v74 offset:12288
	ds_read_b128 v[52:55], v74 offset:13312
	ds_read_b128 v[56:59], v74 offset:14336
	v_pk_add_f32 v[96:97], v[96:97], v[100:101]
	v_pk_add_f32 v[98:99], v[98:99], v[102:103]
	s_nop 1
	v_permlane16_swap_b32_e32 v96, v97
	v_permlane16_swap_b32_e32 v98, v99
	v_add_f32_e32 v96, v96, v97
	v_add_f32_e32 v98, v98, v99
	s_nop 1
	v_permlane32_swap_b32_e32 v96, v98
	v_add_f32_e32 v96, v96, v98
	v_add_f32_e32 v96, v96, v73
	s_waitcnt lgkmcnt(5)
	ds_read_b128 v[60:63], v74 offset:15360
	ds_write_b32 v78, v96
	ds_read2_b32 v[80:81], v79 offset0:0 offset1:4
	ds_read2_b32 v[82:83], v79 offset0:8 offset1:12
	ds_read2_b32 v[84:85], v79 offset0:16 offset1:20
	ds_read2_b32 v[86:87], v79 offset0:24 offset1:28
	ds_read2_b32 v[88:89], v79 offset0:32 offset1:36
	ds_read2_b32 v[90:91], v79 offset0:40 offset1:44
	ds_read2_b32 v[92:93], v79 offset0:48 offset1:52
	ds_read2_b32 v[94:95], v79 offset0:56 offset1:60
	v_lshlrev_b32_e32 v72, 3, v76
	v_lshl_or_b32 v72, v75, 2, v72
	v_cmp_gt_u32_e32 vcc, 2, v75
	s_waitcnt lgkmcnt(0)
	v_pk_mul_f32 v[96:97], v[80:81], v[0:1] op_sel_hi:[0,1]
	v_pk_mul_f32 v[98:99], v[80:81], v[2:3] op_sel_hi:[0,1]
	v_pk_mul_f32 v[100:101], v[80:81], v[4:5] op_sel:[1,0]
	v_pk_mul_f32 v[102:103], v[80:81], v[6:7] op_sel:[1,0]
	v_pk_fma_f32 v[96:97], v[82:83], v[8:9], v[96:97] op_sel_hi:[0,1,1]
	v_pk_fma_f32 v[98:99], v[82:83], v[10:11], v[98:99] op_sel_hi:[0,1,1]
	v_pk_fma_f32 v[100:101], v[82:83], v[12:13], v[100:101] op_sel:[1,0,0]
	v_pk_fma_f32 v[102:103], v[82:83], v[14:15], v[102:103] op_sel:[1,0,0]
	v_pk_fma_f32 v[96:97], v[84:85], v[16:17], v[96:97] op_sel_hi:[0,1,1]
	v_pk_fma_f32 v[98:99], v[84:85], v[18:19], v[98:99] op_sel_hi:[0,1,1]
	v_pk_fma_f32 v[100:101], v[84:85], v[20:21], v[100:101] op_sel:[1,0,0]
	v_pk_fma_f32 v[102:103], v[84:85], v[22:23], v[102:103] op_sel:[1,0,0]
	v_pk_fma_f32 v[96:97], v[86:87], v[24:25], v[96:97] op_sel_hi:[0,1,1]
	v_pk_fma_f32 v[98:99], v[86:87], v[26:27], v[98:99] op_sel_hi:[0,1,1]
	v_pk_fma_f32 v[100:101], v[86:87], v[28:29], v[100:101] op_sel:[1,0,0]
	v_pk_fma_f32 v[102:103], v[86:87], v[30:31], v[102:103] op_sel:[1,0,0]
	v_pk_fma_f32 v[96:97], v[88:89], v[32:33], v[96:97] op_sel_hi:[0,1,1]
	v_pk_fma_f32 v[98:99], v[88:89], v[34:35], v[98:99] op_sel_hi:[0,1,1]
	v_pk_fma_f32 v[100:101], v[88:89], v[36:37], v[100:101] op_sel:[1,0,0]
	v_pk_fma_f32 v[102:103], v[88:89], v[38:39], v[102:103] op_sel:[1,0,0]
	v_pk_fma_f32 v[96:97], v[90:91], v[40:41], v[96:97] op_sel_hi:[0,1,1]
	v_pk_fma_f32 v[98:99], v[90:91], v[42:43], v[98:99] op_sel_hi:[0,1,1]
	v_pk_fma_f32 v[100:101], v[90:91], v[44:45], v[100:101] op_sel:[1,0,0]
	v_pk_fma_f32 v[102:103], v[90:91], v[46:47], v[102:103] op_sel:[1,0,0]
	v_pk_fma_f32 v[96:97], v[92:93], v[48:49], v[96:97] op_sel_hi:[0,1,1]
	v_pk_fma_f32 v[98:99], v[92:93], v[50:51], v[98:99] op_sel_hi:[0,1,1]
	v_pk_fma_f32 v[100:101], v[92:93], v[52:53], v[100:101] op_sel:[1,0,0]
	v_pk_fma_f32 v[102:103], v[92:93], v[54:55], v[102:103] op_sel:[1,0,0]
	v_pk_fma_f32 v[96:97], v[94:95], v[56:57], v[96:97] op_sel_hi:[0,1,1]
	v_pk_fma_f32 v[98:99], v[94:95], v[58:59], v[98:99] op_sel_hi:[0,1,1]
	v_pk_fma_f32 v[100:101], v[94:95], v[60:61], v[100:101] op_sel:[1,0,0]
	v_pk_fma_f32 v[102:103], v[94:95], v[62:63], v[102:103] op_sel:[1,0,0]
	v_pk_add_f32 v[96:97], v[96:97], v[100:101]
	v_pk_add_f32 v[98:99], v[98:99], v[102:103]
	s_nop 1
	v_permlane16_swap_b32_e32 v96, v98
	v_permlane16_swap_b32_e32 v97, v99
	v_add_f32_e32 v96, v96, v98
	v_add_f32_e32 v97, v97, v99
	v_mov_b32_e32 v80, v96
	v_mov_b32_e32 v81, v97
	s_nop 1
	v_permlane32_swap_b32_e32 v96, v80
	v_permlane32_swap_b32_e32 v97, v81
	v_add_f32_e32 v96, v96, v80
	v_add_f32_e32 v97, v97, v81
	v_cvt_pk_f16_f32 v73, v96, v97
	s_and_saveexec_b64 s[4:5], vcc
	global_atomic_pk_add_f16 v72, v73, s[20:21]
	s_endpgm
	.p2align	8
